# dedicated phase-1 converters 6312 tiles, GEMM-in epilogue conversion on the first 6 units only
# speedup vs baseline: 1.0173x; 1.0173x over previous
.LBB0_86:
	s_cmp_lt_i32 s50, 2
	s_cselect_b64 s[6:7], -1, 0
	s_and_b64 s[0:1], s[6:7], s[2:3]
	s_andn2_b64 vcc, exec, s[0:1]
	v_writelane_b32 v254, s60, 4
	s_cbranch_vccnz .LBB0_260
	s_mov_b64 s[2:3], s[80:81]
	s_load_dwordx2 s[8:9], s[2:3], 0xa8
	s_cmpk_lg_i32 s56, 0x100
	s_cselect_b32 s0, s56, 0xc8
	s_cmp_ge_i32 s78, s0
	s_mov_b64 s[4:5], -1
	s_cbranch_scc0 .LBB0_145
	s_sub_i32 s1, s78, s0
	s_cmpk_gt_i32 s1, 0x18a7
	s_cbranch_scc1 .LBB0_144
	s_sub_i32 s20, s56, s0
	s_abs_i32 s4, s20
	v_cvt_f32_u32_e32 v1, s4
	s_load_dwordx2 s[10:11], s[2:3], 0x78
	s_load_dwordx2 s[12:13], s[2:3], 0x88
	s_sub_i32 s2, s20, s1
	s_add_i32 s3, s2, 0x18a7
	v_rcp_iflag_f32_e32 v1, v1
	s_sub_i32 s2, 0xffffe759, s2
	s_xor_b32 s14, s3, s20
	s_sub_i32 s5, 0, s4
	v_mul_f32_e32 v1, 0x4f7ffffe, v1
	v_cvt_u32_f32_e32 v1, v1
	s_max_i32 s2, s3, s2
	s_ashr_i32 s3, s14, 31
	v_readfirstlane_b32 s14, v1
	s_mul_i32 s5, s5, s14
	s_mul_hi_u32 s5, s14, s5
	s_add_i32 s14, s14, s5
	s_mul_hi_u32 s5, s2, s14
	s_mul_i32 s14, s5, s4
	s_sub_i32 s2, s2, s14
	s_add_i32 s14, s5, 1
	s_sub_i32 s15, s2, s4
	s_cmp_ge_u32 s2, s4
	s_cselect_b32 s5, s14, s5
	s_cselect_b32 s2, s15, s2
	s_add_i32 s14, s5, 1
	s_cmp_ge_u32 s2, s4
	s_cselect_b32 s2, s14, s5
	s_xor_b32 s2, s2, s3
	s_sub_i32 s29, s2, s3
	s_lshl_b32 s21, s29, 2
	s_add_i32 s22, s21, -1
	s_cmp_gt_i32 s29, 0
	s_cselect_b64 s[2:3], -1, 0
	s_and_b64 s[4:5], s[2:3], exec
	s_cselect_b32 s18, 0, s22
	s_ashr_i32 s4, s18, 2
	s_mul_i32 s17, s4, s20
	s_add_i32 s17, s17, s1
	s_cmpk_gt_i32 s17, 0x1fff
	s_mov_b32 s5, 0
	s_cbranch_scc0 .LBB0_91
	s_add_i32 s4, s17, 0xffffe000
	s_lshr_b32 s4, s4, 7
	s_lshl_b64 s[4:5], s[4:5], 24
	s_waitcnt lgkmcnt(0)
	s_add_u32 s14, s12, s4
	s_addc_u32 s15, s13, s5
	s_lshl_b32 s4, s17, 4
	s_and_b32 s26, s4, 0x780
	s_lshl_b32 s4, s17, 8
	s_and_b32 s16, s4, 0x700
	s_mov_b64 s[4:5], 0x800
	s_cbranch_execz .LBB0_92
	s_branch .LBB0_93

.LBB0_160:
	s_add_i32 s89, s59, -1
	s_cmp_lt_u32 s89, 6
	s_cselect_b32 s88, 1, 0
	s_cbranch_scc0 .Lp1c_skip1
	s_and_b32 s90, s89, 1
	s_lshr_b32 s91, s57, 2
	s_cmp_eq_u32 s90, s91
	s_cselect_b32 s88, 1, 0
	s_cbranch_scc0 .Lp1c_skip1
	s_lshr_b32 s89, s89, 1
	s_mul_i32 s89, s89, 200
	s_add_u32 s89, s89, s78
	s_add_u32 s89, s89, 6312
	s_cmp_lt_u32 s89, 0x2000
	s_cselect_b32 s88, 1, 0
	s_cbranch_scc0 .Lp1c_skip1
	s_lshr_b32 s90, s89, 4
	s_lshl_b32 s90, s90, 21
	s_and_b32 s91, s89, 15
	s_lshl_b32 s92, s91, 10
	s_or_b32 s90, s90, s92
	s_lshl_b32 s92, s57, 7
	s_or_b32 s90, s90, s92
	s_add_u32 s84, s82, s90
	s_addc_u32 s85, s83, 0
	s_lshr_b32 s90, s89, 8
	s_lshl_b32 s90, s90, 23
	s_lshl_b32 s91, s91, 19
	s_or_b32 s90, s90, s91
	s_bfe_u32 s91, s89, 0x40004
	s_lshl_b32 s91, s91, 7
	s_or_b32 s90, s90, s91
	s_lshl_b32 s91, s57, 15
	s_or_b32 s90, s90, s91
	s_add_u32 s90, s90, 0x4ee00000
	s_add_u32 s86, s48, s90
	s_addc_u32 s87, s49, 0
	global_load_dwordx4 v[180:183], v245, s[84:85] nt
	s_add_u32 s84, s84, 0x4000
	s_addc_u32 s85, s85, 0
	global_load_dwordx4 v[184:187], v245, s[84:85] nt
	s_add_u32 s84, s84, 0x4000
	s_addc_u32 s85, s85, 0
	global_load_dwordx4 v[188:191], v245, s[84:85] nt
	s_add_u32 s84, s84, 0x4000
	s_addc_u32 s85, s85, 0
	global_load_dwordx4 v[192:195], v245, s[84:85] nt
	s_add_u32 s84, s84, 0x4000
	s_addc_u32 s85, s85, 0
	global_load_dwordx4 v[196:199], v245, s[84:85] nt
	s_add_u32 s84, s84, 0x4000
	s_addc_u32 s85, s85, 0
	global_load_dwordx4 v[200:203], v245, s[84:85] nt
	s_add_u32 s84, s84, 0x4000
	s_addc_u32 s85, s85, 0
	global_load_dwordx4 v[204:207], v245, s[84:85] nt
	s_add_u32 s84, s84, 0x4000
	s_addc_u32 s85, s85, 0
	global_load_dwordx4 v[208:211], v245, s[84:85] nt
	s_add_u32 s84, s84, 0x4000
	s_addc_u32 s85, s85, 0
	global_load_dwordx4 v[212:215], v245, s[84:85] nt
	s_add_u32 s84, s84, 0x4000
	s_addc_u32 s85, s85, 0
	global_load_dwordx4 v[216:219], v245, s[84:85] nt
	s_add_u32 s84, s84, 0x4000
	s_addc_u32 s85, s85, 0
	global_load_dwordx4 v[220:223], v245, s[84:85] nt
	s_add_u32 s84, s84, 0x4000
	s_addc_u32 s85, s85, 0
	global_load_dwordx4 v[224:227], v245, s[84:85] nt
	s_add_u32 s84, s84, 0x4000
	s_addc_u32 s85, s85, 0
	global_load_dwordx4 v[228:231], v245, s[84:85] nt
	s_add_u32 s84, s84, 0x4000
	s_addc_u32 s85, s85, 0
	global_load_dwordx4 v[232:235], v245, s[84:85] nt
	s_add_u32 s84, s84, 0x4000
	s_addc_u32 s85, s85, 0
	global_load_dwordx4 v[236:239], v245, s[84:85] nt
	s_add_u32 s84, s84, 0x4000
	s_addc_u32 s85, s85, 0
	global_load_dwordx4 v[240:243], v245, s[84:85] nt
